# L1: octet-broadcast ds_swizzle replaced by DPP row_newbcast movs (VALU), LDS waitcnts re-derived by dataflow
# speedup vs baseline: 1.0094x; 1.0094x over previous
.Lp1_after_idx:
	s_waitcnt vmcnt(0)
	v_lshrrev_b32_e32 v36, 10, v36
	v_lshrrev_b32_e32 v68, 10, v68
	v_lshrrev_b32_e32 v74, 10, v74
	v_lshrrev_b32_e32 v85, 10, v85
	v_lshrrev_b32_e32 v84, 10, v84
	v_lshrrev_b32_e32 v109, 10, v109
	v_lshrrev_b32_e32 v107, 10, v107
	v_lshrrev_b32_e32 v106, 10, v106
	v_lshrrev_b32_e32 v95, 10, v95
	v_and_b32_e32 v36, 0x3fff80, v36
	v_and_b32_e32 v68, 0x3fff80, v68
	v_and_b32_e32 v74, 0x3fff80, v74
	v_and_b32_e32 v85, 0x3fff80, v85
	v_and_b32_e32 v84, 0x3fff80, v84
	v_and_b32_e32 v109, 0x3fff80, v109
	v_and_b32_e32 v107, 0x3fff80, v107
	v_and_b32_e32 v106, 0x3fff80, v106
	v_and_b32_e32 v95, 0x3fff80, v95
	v_mov_b32_dpp v37, v36 row_newbcast:0 row_mask:0xf bank_mask:0x3
	v_mov_b32_dpp v37, v36 row_newbcast:8 row_mask:0xf bank_mask:0xc
	v_mov_b32_dpp v38, v36 row_newbcast:1 row_mask:0xf bank_mask:0x3
	v_mov_b32_dpp v38, v36 row_newbcast:9 row_mask:0xf bank_mask:0xc
	v_mov_b32_dpp v39, v36 row_newbcast:2 row_mask:0xf bank_mask:0x3
	v_mov_b32_dpp v39, v36 row_newbcast:10 row_mask:0xf bank_mask:0xc
	v_mov_b32_dpp v40, v36 row_newbcast:3 row_mask:0xf bank_mask:0x3
	v_mov_b32_dpp v40, v36 row_newbcast:11 row_mask:0xf bank_mask:0xc
	v_mov_b32_dpp v41, v36 row_newbcast:6 row_mask:0xf bank_mask:0x3
	v_mov_b32_dpp v41, v36 row_newbcast:14 row_mask:0xf bank_mask:0xc
	v_add_u32_e32 v37, v102, v37
	v_add_u32_e32 v38, v102, v38
	ds_read_b128 v[60:63], v37 offset:52240
	ds_read_b128 v[52:55], v38 offset:52240
	v_add_u32_e32 v37, v102, v39
	v_mov_b32_dpp v38, v36 row_newbcast:4 row_mask:0xf bank_mask:0x3
	v_mov_b32_dpp v38, v36 row_newbcast:12 row_mask:0xf bank_mask:0xc
	v_add_u32_e32 v39, v102, v40
	v_mov_b32_dpp v40, v36 row_newbcast:5 row_mask:0xf bank_mask:0x3
	v_mov_b32_dpp v40, v36 row_newbcast:13 row_mask:0xf bank_mask:0xc
	v_mov_b32_dpp v42, v36 row_newbcast:7 row_mask:0xf bank_mask:0x3
	v_mov_b32_dpp v42, v36 row_newbcast:15 row_mask:0xf bank_mask:0xc
	ds_read_b128 v[64:67], v37 offset:52240
	ds_read_b128 v[56:59], v39 offset:52240
	v_add_u32_e32 v37, v102, v38
	v_cmp_lt_i32_e32 vcc, 8, v72
	v_add_u32_e32 v36, v102, v40
	v_add_u32_e32 v40, v102, v41
	v_add_u32_e32 v41, v102, v42
	ds_read_b128 v[44:47], v37 offset:52240
	ds_read_b128 v[36:39], v36 offset:52240
	ds_read_b128 v[48:51], v40 offset:52240
	ds_read_b128 v[40:43], v41 offset:52240
	s_cmp_lg_u64 vcc, 0
	s_cselect_b64 s[22:23], -1, 0
	v_cmp_lt_i32_e64 s[6:7], 12, v72
	s_cbranch_vccz .LBB4_44
	v_mov_b32_dpp v0, v68 row_newbcast:0 row_mask:0xf bank_mask:0x3
	v_mov_b32_dpp v0, v68 row_newbcast:8 row_mask:0xf bank_mask:0xc
	v_mov_b32_dpp v1, v68 row_newbcast:1 row_mask:0xf bank_mask:0x3
	v_mov_b32_dpp v1, v68 row_newbcast:9 row_mask:0xf bank_mask:0xc
	v_mov_b32_dpp v16, v68 row_newbcast:2 row_mask:0xf bank_mask:0x3
	v_mov_b32_dpp v16, v68 row_newbcast:10 row_mask:0xf bank_mask:0xc
	v_mov_b32_dpp v17, v68 row_newbcast:3 row_mask:0xf bank_mask:0x3
	v_mov_b32_dpp v17, v68 row_newbcast:11 row_mask:0xf bank_mask:0xc
	v_add_u32_e32 v0, v102, v0
	v_add_u32_e32 v8, v102, v1
	v_add_u32_e32 v16, v102, v16
	v_add_u32_e32 v24, v102, v17
	ds_read_b128 v[0:3], v0 offset:52240
	ds_read_b128 v[8:11], v8 offset:52240
	ds_read_b128 v[16:19], v16 offset:52240
	ds_read_b128 v[24:27], v24 offset:52240
.LBB4_44:
	s_cmp_lg_u64 s[6:7], 0
	s_cselect_b64 s[26:27], -1, 0
	s_cmp_eq_u64 s[6:7], 0
	s_cbranch_scc1 .LBB4_46
	v_mov_b32_dpp v4, v68 row_newbcast:4 row_mask:0xf bank_mask:0x3
	v_mov_b32_dpp v4, v68 row_newbcast:12 row_mask:0xf bank_mask:0xc
	v_mov_b32_dpp v5, v68 row_newbcast:5 row_mask:0xf bank_mask:0x3
	v_mov_b32_dpp v5, v68 row_newbcast:13 row_mask:0xf bank_mask:0xc
	v_mov_b32_dpp v20, v68 row_newbcast:6 row_mask:0xf bank_mask:0x3
	v_mov_b32_dpp v20, v68 row_newbcast:14 row_mask:0xf bank_mask:0xc
	v_mov_b32_dpp v21, v68 row_newbcast:7 row_mask:0xf bank_mask:0x3
	v_mov_b32_dpp v21, v68 row_newbcast:15 row_mask:0xf bank_mask:0xc
	v_add_u32_e32 v4, v102, v4
	v_add_u32_e32 v12, v102, v5
	v_add_u32_e32 v20, v102, v20
	v_add_u32_e32 v28, v102, v21
	ds_read_b128 v[4:7], v4 offset:52240
	ds_read_b128 v[12:15], v12 offset:52240
	ds_read_b128 v[20:23], v20 offset:52240
	ds_read_b128 v[28:31], v28 offset:52240
.LBB4_46:
	v_cvt_f32_i32_e32 v68, v72
	v_max_f32_e32 v68, 1.0, v68
	v_div_scale_f32 v69, s[6:7], v68, v68, 1.0
	v_rcp_f32_e32 v70, v69
	v_div_scale_f32 v71, vcc, 1.0, v68, 1.0
	v_fma_f32 v73, -v69, v70, 1.0
	v_fmac_f32_e32 v70, v73, v70
	v_mul_f32_e32 v73, v71, v70
	v_fma_f32 v75, -v69, v73, v71
	v_fmac_f32_e32 v73, v75, v70
	v_fma_f32 v69, -v69, v73, v71
	v_div_fmas_f32 v69, v69, v70, v73
	v_div_fixup_f32 v68, v69, v68, 1.0
	v_cvt_f16_f32_e32 v69, v68
	v_cvt_pk_f16_f32 v73, v68, v68
	s_andn2_b64 vcc, exec, s[22:23]
	s_waitcnt lgkmcnt(7)
	v_pk_fma_f16 v60, v69, v60, 0 op_sel_hi:[0,1,1]
	v_pk_fma_f16 v61, v69, v61, 0 op_sel_hi:[0,1,1]
	v_pk_fma_f16 v62, v69, v62, 0 op_sel_hi:[0,1,1]
	v_pk_fma_f16 v63, v69, v63, 0 op_sel_hi:[0,1,1]
	s_waitcnt lgkmcnt(6)
	v_pk_fma_f16 v55, v69, v55, v63 op_sel_hi:[0,1,1]
	v_pk_fma_f16 v54, v69, v54, v62 op_sel_hi:[0,1,1]
	v_pk_fma_f16 v53, v69, v53, v61 op_sel_hi:[0,1,1]
	v_pk_fma_f16 v52, v69, v52, v60 op_sel_hi:[0,1,1]
	s_waitcnt lgkmcnt(5)
	v_pk_fma_f16 v52, v69, v64, v52 op_sel_hi:[0,1,1]
	v_pk_fma_f16 v53, v69, v65, v53 op_sel_hi:[0,1,1]
	v_pk_fma_f16 v54, v69, v66, v54 op_sel_hi:[0,1,1]
	v_pk_fma_f16 v55, v69, v67, v55 op_sel_hi:[0,1,1]
	s_waitcnt lgkmcnt(4)
	v_pk_fma_f16 v55, v69, v59, v55 op_sel_hi:[0,1,1]
	v_pk_fma_f16 v54, v69, v58, v54 op_sel_hi:[0,1,1]
	v_pk_fma_f16 v53, v69, v57, v53 op_sel_hi:[0,1,1]
	v_pk_fma_f16 v52, v69, v56, v52 op_sel_hi:[0,1,1]
	s_waitcnt lgkmcnt(3)
	v_pk_fma_f16 v52, v69, v44, v52 op_sel_hi:[0,1,1]
	v_pk_fma_f16 v53, v69, v45, v53 op_sel_hi:[0,1,1]
	v_pk_fma_f16 v54, v69, v46, v54 op_sel_hi:[0,1,1]
	v_pk_fma_f16 v55, v69, v47, v55 op_sel_hi:[0,1,1]
	s_waitcnt lgkmcnt(2)
	v_pk_fma_f16 v55, v69, v39, v55 op_sel_hi:[0,1,1]
	v_pk_fma_f16 v54, v69, v38, v54 op_sel_hi:[0,1,1]
	v_pk_fma_f16 v53, v69, v37, v53 op_sel_hi:[0,1,1]
	v_pk_fma_f16 v52, v69, v36, v52 op_sel_hi:[0,1,1]
	s_waitcnt lgkmcnt(1)
	v_pk_fma_f16 v52, v69, v48, v52 op_sel_hi:[0,1,1]
	v_pk_fma_f16 v53, v69, v49, v53 op_sel_hi:[0,1,1]
	v_pk_fma_f16 v54, v69, v50, v54 op_sel_hi:[0,1,1]
	v_pk_fma_f16 v55, v69, v51, v55 op_sel_hi:[0,1,1]
	s_waitcnt lgkmcnt(0)
	v_pk_fma_f16 v55, v69, v43, v55 op_sel_hi:[0,1,1]
	v_pk_fma_f16 v54, v69, v42, v54 op_sel_hi:[0,1,1]
	v_pk_fma_f16 v53, v69, v41, v53 op_sel_hi:[0,1,1]
	v_pk_fma_f16 v52, v69, v40, v52 op_sel_hi:[0,1,1]
	s_cbranch_vccnz .LBB4_48
	v_pk_fma_f16 v52, v73, v0, v52
	v_pk_fma_f16 v53, v73, v1, v53
	v_pk_fma_f16 v54, v73, v2, v54
	v_pk_fma_f16 v55, v73, v3, v55
	v_pk_fma_f16 v54, v73, v10, v54
	v_pk_fma_f16 v55, v73, v11, v55
	v_pk_fma_f16 v53, v73, v9, v53
	v_pk_fma_f16 v52, v73, v8, v52
	v_pk_fma_f16 v53, v73, v17, v53
	v_pk_fma_f16 v52, v73, v16, v52
	v_pk_fma_f16 v54, v73, v18, v54
	v_pk_fma_f16 v55, v73, v19, v55
	v_pk_fma_f16 v54, v73, v26, v54
	v_pk_fma_f16 v55, v73, v27, v55
	v_pk_fma_f16 v53, v73, v25, v53
	v_pk_fma_f16 v52, v73, v24, v52

.LBB4_50:
	v_cmp_lt_i32_e32 vcc, 16, v72
	s_cbranch_vccz .LBB4_61
	v_mov_b32_dpp v56, v74 row_newbcast:0 row_mask:0xf bank_mask:0x3
	v_mov_b32_dpp v56, v74 row_newbcast:8 row_mask:0xf bank_mask:0xc
	v_mov_b32_dpp v57, v74 row_newbcast:1 row_mask:0xf bank_mask:0x3
	v_mov_b32_dpp v57, v74 row_newbcast:9 row_mask:0xf bank_mask:0xc
	v_mov_b32_dpp v58, v74 row_newbcast:2 row_mask:0xf bank_mask:0x3
	v_mov_b32_dpp v58, v74 row_newbcast:10 row_mask:0xf bank_mask:0xc
	v_mov_b32_dpp v59, v74 row_newbcast:3 row_mask:0xf bank_mask:0x3
	v_mov_b32_dpp v59, v74 row_newbcast:11 row_mask:0xf bank_mask:0xc
	v_cmp_lt_i32_e32 vcc, 20, v72
	v_add_u32_e32 v56, v102, v56
	v_add_u32_e32 v57, v102, v57
	ds_read_b128 v[68:71], v56 offset:52240
	ds_read_b128 v[64:67], v57 offset:52240
	v_add_u32_e32 v56, v102, v58
	v_add_u32_e32 v57, v102, v59
	ds_read_b128 v[60:63], v56 offset:52240
	ds_read_b128 v[56:59], v57 offset:52240
	s_cmp_lg_u64 vcc, 0
	s_cselect_b64 s[6:7], -1, 0
	s_cbranch_vccz .LBB4_53
	v_mov_b32_dpp v36, v74 row_newbcast:4 row_mask:0xf bank_mask:0x3
	v_mov_b32_dpp v36, v74 row_newbcast:12 row_mask:0xf bank_mask:0xc
	v_mov_b32_dpp v37, v74 row_newbcast:5 row_mask:0xf bank_mask:0x3
	v_mov_b32_dpp v37, v74 row_newbcast:13 row_mask:0xf bank_mask:0xc
	v_mov_b32_dpp v40, v74 row_newbcast:6 row_mask:0xf bank_mask:0x3
	v_mov_b32_dpp v40, v74 row_newbcast:14 row_mask:0xf bank_mask:0xc
	v_mov_b32_dpp v41, v74 row_newbcast:7 row_mask:0xf bank_mask:0x3
	v_mov_b32_dpp v41, v74 row_newbcast:15 row_mask:0xf bank_mask:0xc
	v_add_u32_e32 v36, v102, v36
	v_add_u32_e32 v37, v102, v37
	v_add_u32_e32 v40, v102, v40
	v_add_u32_e32 v41, v102, v41
	ds_read_b128 v[44:47], v36 offset:52240
	ds_read_b128 v[36:39], v37 offset:52240
	ds_read_b128 v[48:51], v40 offset:52240
	ds_read_b128 v[40:43], v41 offset:52240

.LBB4_56:
	s_waitcnt lgkmcnt(0)
	s_or_b64 exec, exec, s[6:7]
	s_nop 1
	v_mov_b32_dpp v37, v36 row_newbcast:0 row_mask:0xf bank_mask:0x3
	v_mov_b32_dpp v37, v36 row_newbcast:8 row_mask:0xf bank_mask:0xc
	v_mov_b32_dpp v38, v36 row_newbcast:1 row_mask:0xf bank_mask:0x3
	v_mov_b32_dpp v38, v36 row_newbcast:9 row_mask:0xf bank_mask:0xc
	v_mov_b32_dpp v46, v36 row_newbcast:2 row_mask:0xf bank_mask:0x3
	v_mov_b32_dpp v46, v36 row_newbcast:10 row_mask:0xf bank_mask:0xc
	v_mov_b32_dpp v47, v36 row_newbcast:3 row_mask:0xf bank_mask:0x3
	v_mov_b32_dpp v47, v36 row_newbcast:11 row_mask:0xf bank_mask:0xc
	v_mov_b32_dpp v50, v36 row_newbcast:4 row_mask:0xf bank_mask:0x3
	v_mov_b32_dpp v50, v36 row_newbcast:12 row_mask:0xf bank_mask:0xc
	v_add_u32_e32 v37, v102, v37
	v_add_u32_e32 v42, v102, v38
	ds_read_b128 v[38:41], v37 offset:52240
	ds_read_b128 v[42:45], v42 offset:52240
	v_add_u32_e32 v37, v102, v46
	v_add_u32_e32 v51, v102, v47
	v_mov_b32_dpp v60, v36 row_newbcast:5 row_mask:0xf bank_mask:0x3
	v_mov_b32_dpp v60, v36 row_newbcast:13 row_mask:0xf bank_mask:0xc
	ds_read_b128 v[46:49], v37 offset:52240
	ds_read_b128 v[56:59], v51 offset:52240
	v_add_u32_e32 v37, v102, v50
	v_mov_b32_dpp v50, v36 row_newbcast:6 row_mask:0xf bank_mask:0x3
	v_mov_b32_dpp v50, v36 row_newbcast:14 row_mask:0xf bank_mask:0xc
	v_mov_b32_dpp v36, v36 row_newbcast:7 row_mask:0xf bank_mask:0x3
	v_mov_b32_dpp v36, v36 row_newbcast:15 row_mask:0xf bank_mask:0xc
	v_add_u32_e32 v51, v102, v60
	ds_read_b128 v[60:63], v37 offset:52240
	ds_read_b128 v[64:67], v51 offset:52240
	s_add_i32 s22, s22, 8
	v_add_u32_e32 v37, v102, v50
	v_add_u32_e32 v36, v102, v36
	ds_read_b128 v[68:71], v37 offset:52240
	ds_read_b128 v[74:77], v36 offset:52240
	s_waitcnt lgkmcnt(7)
	v_pk_fma_f16 v36, v73, v38, v52
	v_pk_fma_f16 v37, v73, v39, v53
	v_pk_fma_f16 v38, v73, v40, v54
	v_pk_fma_f16 v39, v73, v41, v55
	s_waitcnt lgkmcnt(6)
	v_pk_fma_f16 v38, v73, v44, v38
	v_pk_fma_f16 v39, v73, v45, v39
	v_pk_fma_f16 v37, v73, v43, v37
	v_pk_fma_f16 v36, v73, v42, v36
	s_waitcnt lgkmcnt(5)
	v_pk_fma_f16 v37, v73, v47, v37
	v_pk_fma_f16 v36, v73, v46, v36
	v_pk_fma_f16 v38, v73, v48, v38
	v_pk_fma_f16 v39, v73, v49, v39
	s_waitcnt lgkmcnt(4)
	v_pk_fma_f16 v38, v73, v58, v38
	v_pk_fma_f16 v39, v73, v59, v39
	v_pk_fma_f16 v37, v73, v57, v37
	v_pk_fma_f16 v36, v73, v56, v36
	s_waitcnt lgkmcnt(3)
	v_pk_fma_f16 v37, v73, v61, v37
	v_pk_fma_f16 v36, v73, v60, v36
	v_pk_fma_f16 v38, v73, v62, v38
	v_pk_fma_f16 v39, v73, v63, v39
	s_waitcnt lgkmcnt(2)
	v_pk_fma_f16 v38, v73, v66, v38
	v_pk_fma_f16 v39, v73, v67, v39
	v_pk_fma_f16 v37, v73, v65, v37
	v_pk_fma_f16 v36, v73, v64, v36
	s_waitcnt lgkmcnt(1)
	v_pk_fma_f16 v37, v73, v69, v37
	v_pk_fma_f16 v36, v73, v68, v36
	v_pk_fma_f16 v38, v73, v70, v38
	v_pk_fma_f16 v39, v73, v71, v39
	s_waitcnt lgkmcnt(0)
	v_pk_fma_f16 v54, v73, v76, v38
	v_pk_fma_f16 v55, v73, v77, v39
	v_pk_fma_f16 v53, v73, v75, v37
	v_pk_fma_f16 v52, v73, v74, v36
.LBB4_57:
	s_waitcnt lgkmcnt(0)
	v_cmp_lt_i32_e32 vcc, s22, v72
	s_cbranch_vccz .LBB4_60
	v_add_u32_e32 v36, s22, v97
	v_cmp_lt_i32_e32 vcc, v36, v72
	v_mov_b32_e32 v36, 0x10000
	s_and_saveexec_b64 s[6:7], vcc
	s_cbranch_execz .LBB4_56
	v_add_u32_e32 v36, s22, v32
	v_ashrrev_i32_e32 v37, 31, v36
	v_lshl_add_u64 v[36:37], v[36:37], 2, s[12:13]
	global_load_dword v36, v[36:37], off
	s_waitcnt vmcnt(0)
	v_lshrrev_b32_e32 v36, 10, v36
	v_and_b32_e32 v36, 0x3fff80, v36
	s_branch .LBB4_56

.LBB4_61:
	ds_write_b128 v104, v[52:55] offset:33792
	ds_read_b128 v[36:39], v105
	ds_read_b128 v[40:43], v103 offset:33792
	ds_read_b128 v[44:47], v105 offset:8448
	ds_read_b128 v[48:51], v105 offset:16896
	ds_read_b128 v[52:55], v105 offset:25344
	s_waitcnt lgkmcnt(3)
	v_mfma_f32_16x16x32_f16 v[36:39], v[36:39], v[40:43], 0
	s_waitcnt lgkmcnt(2)
	v_mfma_f32_16x16x32_f16 v[44:47], v[44:47], v[40:43], 0
	s_waitcnt lgkmcnt(1)
	v_mfma_f32_16x16x32_f16 v[48:51], v[48:51], v[40:43], 0
	s_waitcnt lgkmcnt(0)
	v_mfma_f32_16x16x32_f16 v[52:55], v[52:55], v[40:43], 0
	ds_read_b128 v[40:43], v105 offset:64
	ds_read_b128 v[56:59], v103 offset:33856
	ds_read_b128 v[60:63], v105 offset:8512
	ds_read_b128 v[64:67], v105 offset:16960
	v_mov_b32_dpp v32, v85 row_newbcast:0 row_mask:0xf bank_mask:0x3
	v_mov_b32_dpp v32, v85 row_newbcast:8 row_mask:0xf bank_mask:0xc
	v_mov_b32_dpp v72, v85 row_newbcast:1 row_mask:0xf bank_mask:0x3
	v_mov_b32_dpp v72, v85 row_newbcast:9 row_mask:0xf bank_mask:0xc
	s_waitcnt lgkmcnt(2)
	v_mfma_f32_16x16x32_f16 v[36:39], v[40:43], v[56:59], v[36:39]
	v_cmp_lt_i32_e32 vcc, 8, v108
	s_cmp_lg_u64 vcc, 0
	v_add_u32_e32 v32, v102, v32
	s_waitcnt lgkmcnt(1)
	v_mfma_f32_16x16x32_f16 v[40:43], v[60:63], v[56:59], v[44:47]
	ds_read_b128 v[60:63], v105 offset:25408
	ds_read_b128 v[68:71], v32 offset:52240
	v_mov_b32_dpp v32, v85 row_newbcast:2 row_mask:0xf bank_mask:0x3
	v_mov_b32_dpp v32, v85 row_newbcast:10 row_mask:0xf bank_mask:0xc
	s_waitcnt lgkmcnt(2)
	v_mfma_f32_16x16x32_f16 v[44:47], v[64:67], v[56:59], v[48:51]
	v_add_u32_e32 v64, v102, v72
	s_cselect_b64 s[22:23], -1, 0
	v_cmp_lt_i32_e64 s[6:7], 12, v108
	s_waitcnt lgkmcnt(1)
	v_mfma_f32_16x16x32_f16 v[48:51], v[60:63], v[56:59], v[52:55]
	v_add_u32_e32 v32, v102, v32
	s_nop 0
	v_mov_b32_dpp v52, v85 row_newbcast:3 row_mask:0xf bank_mask:0x3
	v_mov_b32_dpp v52, v85 row_newbcast:11 row_mask:0xf bank_mask:0xc
	v_mov_b32_dpp v53, v85 row_newbcast:4 row_mask:0xf bank_mask:0x3
	v_mov_b32_dpp v53, v85 row_newbcast:12 row_mask:0xf bank_mask:0xc
	ds_read_b128 v[76:79], v64 offset:52240
	ds_read_b128 v[72:75], v32 offset:52240
	v_mov_b32_dpp v56, v85 row_newbcast:5 row_mask:0xf bank_mask:0x3
	v_mov_b32_dpp v56, v85 row_newbcast:13 row_mask:0xf bank_mask:0xc
	v_mov_b32_dpp v57, v85 row_newbcast:6 row_mask:0xf bank_mask:0x3
	v_mov_b32_dpp v57, v85 row_newbcast:14 row_mask:0xf bank_mask:0xc
	v_add_u32_e32 v32, v102, v52
	v_add_u32_e32 v52, v102, v53
	ds_read_b128 v[80:83], v32 offset:52240
	ds_read_b128 v[52:55], v52 offset:52240
	v_mov_b32_dpp v32, v85 row_newbcast:7 row_mask:0xf bank_mask:0x3
	v_mov_b32_dpp v32, v85 row_newbcast:15 row_mask:0xf bank_mask:0xc
	v_add_u32_e32 v56, v102, v56
	v_add_u32_e32 v57, v102, v57
	ds_read_b128 v[60:63], v56 offset:52240
	ds_read_b128 v[64:67], v57 offset:52240
	v_add_u32_e32 v32, v102, v32
	ds_read_b128 v[56:59], v32 offset:52240
	s_cbranch_vccz .LBB4_63
	v_mov_b32_dpp v0, v84 row_newbcast:0 row_mask:0xf bank_mask:0x3
	v_mov_b32_dpp v0, v84 row_newbcast:8 row_mask:0xf bank_mask:0xc
	v_mov_b32_dpp v1, v84 row_newbcast:1 row_mask:0xf bank_mask:0x3
	v_mov_b32_dpp v1, v84 row_newbcast:9 row_mask:0xf bank_mask:0xc
	v_mov_b32_dpp v16, v84 row_newbcast:2 row_mask:0xf bank_mask:0x3
	v_mov_b32_dpp v16, v84 row_newbcast:10 row_mask:0xf bank_mask:0xc
	v_mov_b32_dpp v17, v84 row_newbcast:3 row_mask:0xf bank_mask:0x3
	v_mov_b32_dpp v17, v84 row_newbcast:11 row_mask:0xf bank_mask:0xc
	v_add_u32_e32 v0, v102, v0
	v_add_u32_e32 v8, v102, v1
	v_add_u32_e32 v16, v102, v16
	v_add_u32_e32 v24, v102, v17
	ds_read_b128 v[0:3], v0 offset:52240
	ds_read_b128 v[8:11], v8 offset:52240
	ds_read_b128 v[16:19], v16 offset:52240
	ds_read_b128 v[24:27], v24 offset:52240
.LBB4_63:
	s_cmp_lg_u64 s[6:7], 0
	s_cselect_b64 s[26:27], -1, 0
	s_cmp_eq_u64 s[6:7], 0
	s_cbranch_scc1 .LBB4_65
	v_mov_b32_dpp v4, v84 row_newbcast:4 row_mask:0xf bank_mask:0x3
	v_mov_b32_dpp v4, v84 row_newbcast:12 row_mask:0xf bank_mask:0xc
	v_mov_b32_dpp v5, v84 row_newbcast:5 row_mask:0xf bank_mask:0x3
	v_mov_b32_dpp v5, v84 row_newbcast:13 row_mask:0xf bank_mask:0xc
	v_mov_b32_dpp v20, v84 row_newbcast:6 row_mask:0xf bank_mask:0x3
	v_mov_b32_dpp v20, v84 row_newbcast:14 row_mask:0xf bank_mask:0xc
	v_mov_b32_dpp v21, v84 row_newbcast:7 row_mask:0xf bank_mask:0x3
	v_mov_b32_dpp v21, v84 row_newbcast:15 row_mask:0xf bank_mask:0xc
	v_add_u32_e32 v4, v102, v4
	v_add_u32_e32 v12, v102, v5
	v_add_u32_e32 v20, v102, v20
	v_add_u32_e32 v28, v102, v21
	ds_read_b128 v[4:7], v4 offset:52240
	ds_read_b128 v[12:15], v12 offset:52240
	ds_read_b128 v[20:23], v20 offset:52240
	ds_read_b128 v[28:31], v28 offset:52240
.LBB4_65:
	v_cvt_f32_i32_e32 v32, v108
	v_max_f32_e32 v32, 1.0, v32
	v_div_scale_f32 v84, s[6:7], v32, v32, 1.0
	v_rcp_f32_e32 v85, v84
	v_div_scale_f32 v86, vcc, 1.0, v32, 1.0
	v_fma_f32 v87, -v84, v85, 1.0
	v_fmac_f32_e32 v85, v87, v85
	v_mul_f32_e32 v87, v86, v85
	v_fma_f32 v110, -v84, v87, v86
	v_fmac_f32_e32 v87, v110, v85
	v_fma_f32 v84, -v84, v87, v86
	v_div_fmas_f32 v84, v84, v85, v87
	v_div_fixup_f32 v32, v84, v32, 1.0
	v_cvt_f16_f32_e32 v84, v32
	v_cvt_pk_f16_f32 v32, v32, v32
	s_andn2_b64 vcc, exec, s[22:23]
	s_waitcnt lgkmcnt(7)
	v_pk_fma_f16 v68, v84, v68, 0 op_sel_hi:[0,1,1]
	v_pk_fma_f16 v69, v84, v69, 0 op_sel_hi:[0,1,1]
	v_pk_fma_f16 v70, v84, v70, 0 op_sel_hi:[0,1,1]
	v_pk_fma_f16 v71, v84, v71, 0 op_sel_hi:[0,1,1]
	s_waitcnt lgkmcnt(6)
	v_pk_fma_f16 v71, v84, v79, v71 op_sel_hi:[0,1,1]
	v_pk_fma_f16 v70, v84, v78, v70 op_sel_hi:[0,1,1]
	v_pk_fma_f16 v69, v84, v77, v69 op_sel_hi:[0,1,1]
	v_pk_fma_f16 v68, v84, v76, v68 op_sel_hi:[0,1,1]
	s_waitcnt lgkmcnt(5)
	v_pk_fma_f16 v68, v84, v72, v68 op_sel_hi:[0,1,1]
	v_pk_fma_f16 v69, v84, v73, v69 op_sel_hi:[0,1,1]
	v_pk_fma_f16 v70, v84, v74, v70 op_sel_hi:[0,1,1]
	v_pk_fma_f16 v71, v84, v75, v71 op_sel_hi:[0,1,1]
	s_waitcnt lgkmcnt(4)
	v_pk_fma_f16 v71, v84, v83, v71 op_sel_hi:[0,1,1]
	v_pk_fma_f16 v70, v84, v82, v70 op_sel_hi:[0,1,1]
	v_pk_fma_f16 v69, v84, v81, v69 op_sel_hi:[0,1,1]
	v_pk_fma_f16 v68, v84, v80, v68 op_sel_hi:[0,1,1]
	s_waitcnt lgkmcnt(3)
	v_pk_fma_f16 v68, v84, v52, v68 op_sel_hi:[0,1,1]
	v_pk_fma_f16 v69, v84, v53, v69 op_sel_hi:[0,1,1]
	v_pk_fma_f16 v70, v84, v54, v70 op_sel_hi:[0,1,1]
	v_pk_fma_f16 v71, v84, v55, v71 op_sel_hi:[0,1,1]
	s_waitcnt lgkmcnt(2)
	v_pk_fma_f16 v71, v84, v63, v71 op_sel_hi:[0,1,1]
	v_pk_fma_f16 v70, v84, v62, v70 op_sel_hi:[0,1,1]
	v_pk_fma_f16 v69, v84, v61, v69 op_sel_hi:[0,1,1]
	v_pk_fma_f16 v68, v84, v60, v68 op_sel_hi:[0,1,1]
	s_waitcnt lgkmcnt(1)
	v_pk_fma_f16 v68, v84, v64, v68 op_sel_hi:[0,1,1]
	v_pk_fma_f16 v69, v84, v65, v69 op_sel_hi:[0,1,1]
	v_pk_fma_f16 v70, v84, v66, v70 op_sel_hi:[0,1,1]
	v_pk_fma_f16 v71, v84, v67, v71 op_sel_hi:[0,1,1]
	s_waitcnt lgkmcnt(0)
	v_pk_fma_f16 v71, v84, v59, v71 op_sel_hi:[0,1,1]
	v_pk_fma_f16 v70, v84, v58, v70 op_sel_hi:[0,1,1]
	v_pk_fma_f16 v69, v84, v57, v69 op_sel_hi:[0,1,1]
	v_pk_fma_f16 v68, v84, v56, v68 op_sel_hi:[0,1,1]
	s_cbranch_vccnz .LBB4_67
	v_pk_fma_f16 v68, v32, v0, v68
	v_pk_fma_f16 v69, v32, v1, v69
	v_pk_fma_f16 v70, v32, v2, v70
	v_pk_fma_f16 v71, v32, v3, v71
	v_pk_fma_f16 v70, v32, v10, v70
	v_pk_fma_f16 v71, v32, v11, v71
	v_pk_fma_f16 v69, v32, v9, v69
	v_pk_fma_f16 v68, v32, v8, v68
	v_pk_fma_f16 v69, v32, v17, v69
	v_pk_fma_f16 v68, v32, v16, v68
	v_pk_fma_f16 v70, v32, v18, v70
	v_pk_fma_f16 v71, v32, v19, v71
	v_pk_fma_f16 v70, v32, v26, v70
	v_pk_fma_f16 v71, v32, v27, v71
	v_pk_fma_f16 v69, v32, v25, v69
	v_pk_fma_f16 v68, v32, v24, v68

.LBB4_69:
	v_cmp_lt_i32_e32 vcc, 16, v108
	s_cbranch_vccz .LBB4_80
	v_mov_b32_dpp v72, v109 row_newbcast:0 row_mask:0xf bank_mask:0x3
	v_mov_b32_dpp v72, v109 row_newbcast:8 row_mask:0xf bank_mask:0xc
	v_mov_b32_dpp v73, v109 row_newbcast:1 row_mask:0xf bank_mask:0x3
	v_mov_b32_dpp v73, v109 row_newbcast:9 row_mask:0xf bank_mask:0xc
	v_mov_b32_dpp v74, v109 row_newbcast:2 row_mask:0xf bank_mask:0x3
	v_mov_b32_dpp v74, v109 row_newbcast:10 row_mask:0xf bank_mask:0xc
	v_mov_b32_dpp v75, v109 row_newbcast:3 row_mask:0xf bank_mask:0x3
	v_mov_b32_dpp v75, v109 row_newbcast:11 row_mask:0xf bank_mask:0xc
	v_cmp_lt_i32_e32 vcc, 20, v108
	v_add_u32_e32 v72, v102, v72
	v_add_u32_e32 v73, v102, v73
	ds_read_b128 v[84:87], v72 offset:52240
	ds_read_b128 v[80:83], v73 offset:52240
	v_add_u32_e32 v72, v102, v74
	v_add_u32_e32 v73, v102, v75
	ds_read_b128 v[76:79], v72 offset:52240
	ds_read_b128 v[72:75], v73 offset:52240
	s_cmp_lg_u64 vcc, 0
	s_cselect_b64 s[6:7], -1, 0
	s_cbranch_vccz .LBB4_72
	v_mov_b32_dpp v52, v109 row_newbcast:4 row_mask:0xf bank_mask:0x3
	v_mov_b32_dpp v52, v109 row_newbcast:12 row_mask:0xf bank_mask:0xc
	v_mov_b32_dpp v53, v109 row_newbcast:5 row_mask:0xf bank_mask:0x3
	v_mov_b32_dpp v53, v109 row_newbcast:13 row_mask:0xf bank_mask:0xc
	v_mov_b32_dpp v56, v109 row_newbcast:6 row_mask:0xf bank_mask:0x3
	v_mov_b32_dpp v56, v109 row_newbcast:14 row_mask:0xf bank_mask:0xc
	v_mov_b32_dpp v57, v109 row_newbcast:7 row_mask:0xf bank_mask:0x3
	v_mov_b32_dpp v57, v109 row_newbcast:15 row_mask:0xf bank_mask:0xc
	v_add_u32_e32 v52, v102, v52
	v_add_u32_e32 v58, v102, v53
	v_add_u32_e32 v56, v102, v56
	v_add_u32_e32 v57, v102, v57
	ds_read_b128 v[52:55], v52 offset:52240
	ds_read_b128 v[60:63], v58 offset:52240
	ds_read_b128 v[64:67], v56 offset:52240
	ds_read_b128 v[56:59], v57 offset:52240

.LBB4_75:
	s_waitcnt lgkmcnt(0)
	s_or_b64 exec, exec, s[6:7]
	s_nop 1
	v_mov_b32_dpp v53, v52 row_newbcast:0 row_mask:0xf bank_mask:0x3
	v_mov_b32_dpp v53, v52 row_newbcast:8 row_mask:0xf bank_mask:0xc
	v_mov_b32_dpp v54, v52 row_newbcast:1 row_mask:0xf bank_mask:0x3
	v_mov_b32_dpp v54, v52 row_newbcast:9 row_mask:0xf bank_mask:0xc
	v_mov_b32_dpp v62, v52 row_newbcast:2 row_mask:0xf bank_mask:0x3
	v_mov_b32_dpp v62, v52 row_newbcast:10 row_mask:0xf bank_mask:0xc
	v_mov_b32_dpp v63, v52 row_newbcast:3 row_mask:0xf bank_mask:0x3
	v_mov_b32_dpp v63, v52 row_newbcast:11 row_mask:0xf bank_mask:0xc
	v_mov_b32_dpp v66, v52 row_newbcast:4 row_mask:0xf bank_mask:0x3
	v_mov_b32_dpp v66, v52 row_newbcast:12 row_mask:0xf bank_mask:0xc
	v_add_u32_e32 v53, v102, v53
	v_add_u32_e32 v58, v102, v54
	ds_read_b128 v[54:57], v53 offset:52240
	ds_read_b128 v[58:61], v58 offset:52240
	v_add_u32_e32 v53, v102, v62
	v_add_u32_e32 v67, v102, v63
	v_mov_b32_dpp v76, v52 row_newbcast:5 row_mask:0xf bank_mask:0x3
	v_mov_b32_dpp v76, v52 row_newbcast:13 row_mask:0xf bank_mask:0xc
	ds_read_b128 v[62:65], v53 offset:52240
	ds_read_b128 v[72:75], v67 offset:52240
	v_add_u32_e32 v53, v102, v66
	v_mov_b32_dpp v66, v52 row_newbcast:6 row_mask:0xf bank_mask:0x3
	v_mov_b32_dpp v66, v52 row_newbcast:14 row_mask:0xf bank_mask:0xc
	v_mov_b32_dpp v52, v52 row_newbcast:7 row_mask:0xf bank_mask:0x3
	v_mov_b32_dpp v52, v52 row_newbcast:15 row_mask:0xf bank_mask:0xc
	v_add_u32_e32 v67, v102, v76
	ds_read_b128 v[76:79], v53 offset:52240
	ds_read_b128 v[80:83], v67 offset:52240
	s_add_i32 s22, s22, 8
	v_add_u32_e32 v53, v102, v66
	v_add_u32_e32 v52, v102, v52
	ds_read_b128 v[84:87], v53 offset:52240
	ds_read_b128 v[110:113], v52 offset:52240
	s_waitcnt lgkmcnt(7)
	v_pk_fma_f16 v52, v32, v54, v68
	v_pk_fma_f16 v53, v32, v55, v69
	v_pk_fma_f16 v54, v32, v56, v70
	v_pk_fma_f16 v55, v32, v57, v71
	s_waitcnt lgkmcnt(6)
	v_pk_fma_f16 v54, v32, v60, v54
	v_pk_fma_f16 v55, v32, v61, v55
	v_pk_fma_f16 v53, v32, v59, v53
	v_pk_fma_f16 v52, v32, v58, v52
	s_waitcnt lgkmcnt(5)
	v_pk_fma_f16 v53, v32, v63, v53
	v_pk_fma_f16 v52, v32, v62, v52
	v_pk_fma_f16 v54, v32, v64, v54
	v_pk_fma_f16 v55, v32, v65, v55
	s_waitcnt lgkmcnt(4)
	v_pk_fma_f16 v54, v32, v74, v54
	v_pk_fma_f16 v55, v32, v75, v55
	v_pk_fma_f16 v53, v32, v73, v53
	v_pk_fma_f16 v52, v32, v72, v52
	s_waitcnt lgkmcnt(3)
	v_pk_fma_f16 v53, v32, v77, v53
	v_pk_fma_f16 v52, v32, v76, v52
	v_pk_fma_f16 v54, v32, v78, v54
	v_pk_fma_f16 v55, v32, v79, v55
	s_waitcnt lgkmcnt(2)
	v_pk_fma_f16 v54, v32, v82, v54
	v_pk_fma_f16 v55, v32, v83, v55
	v_pk_fma_f16 v53, v32, v81, v53
	v_pk_fma_f16 v52, v32, v80, v52
	s_waitcnt lgkmcnt(1)
	v_pk_fma_f16 v53, v32, v85, v53
	v_pk_fma_f16 v52, v32, v84, v52
	v_pk_fma_f16 v54, v32, v86, v54
	v_pk_fma_f16 v55, v32, v87, v55
	s_waitcnt lgkmcnt(0)
	v_pk_fma_f16 v70, v32, v112, v54
	v_pk_fma_f16 v71, v32, v113, v55
	v_pk_fma_f16 v69, v32, v111, v53
	v_pk_fma_f16 v68, v32, v110, v52
.LBB4_76:
	s_waitcnt lgkmcnt(0)
	v_cmp_lt_i32_e32 vcc, s22, v108
	s_cbranch_vccz .LBB4_79
	v_add_u32_e32 v52, s22, v97
	v_cmp_lt_i32_e32 vcc, v52, v108
	v_mov_b32_e32 v52, 0x10000
	s_and_saveexec_b64 s[6:7], vcc
	s_cbranch_execz .LBB4_75
	v_add_u32_e32 v52, s22, v33
	v_ashrrev_i32_e32 v53, 31, v52
	v_lshl_add_u64 v[52:53], v[52:53], 2, s[12:13]
	global_load_dword v52, v[52:53], off
	s_waitcnt vmcnt(0)
	v_lshrrev_b32_e32 v52, 10, v52
	v_and_b32_e32 v52, 0x3fff80, v52
	s_branch .LBB4_75

.LBB4_80:
	ds_write_b128 v104, v[68:71] offset:33792
	ds_read_b128 v[52:55], v105 offset:128
	ds_read_b128 v[56:59], v103 offset:33792
	ds_read_b128 v[60:63], v105 offset:8576
	s_waitcnt lgkmcnt(1)
	v_mfma_f32_16x16x32_f16 v[36:39], v[52:55], v[56:59], v[36:39]
	ds_read_b128 v[52:55], v105 offset:17024
	s_waitcnt lgkmcnt(1)
	v_mfma_f32_16x16x32_f16 v[40:43], v[60:63], v[56:59], v[40:43]
	s_waitcnt lgkmcnt(0)
	v_mfma_f32_16x16x32_f16 v[44:47], v[52:55], v[56:59], v[44:47]
	ds_read_b128 v[52:55], v105 offset:25472
	s_waitcnt lgkmcnt(0)
	v_mfma_f32_16x16x32_f16 v[48:51], v[52:55], v[56:59], v[48:51]
	ds_read_b128 v[52:55], v105 offset:192
	ds_read_b128 v[56:59], v103 offset:33856
	ds_read_b128 v[60:63], v105 offset:8640
	v_mov_b32_dpp v32, v107 row_newbcast:0 row_mask:0xf bank_mask:0x3
	v_mov_b32_dpp v32, v107 row_newbcast:8 row_mask:0xf bank_mask:0xc
	v_mov_b32_dpp v33, v107 row_newbcast:1 row_mask:0xf bank_mask:0x3
	v_mov_b32_dpp v33, v107 row_newbcast:9 row_mask:0xf bank_mask:0xc
	v_cmp_lt_i32_e32 vcc, 8, v35
	s_waitcnt lgkmcnt(1)
	v_mfma_f32_16x16x32_f16 v[36:39], v[52:55], v[56:59], v[36:39]
	ds_read_b128 v[52:55], v105 offset:17088
	v_add_u32_e32 v32, v102, v32
	ds_read_b128 v[68:71], v32 offset:52240
	s_waitcnt lgkmcnt(2)
	v_mfma_f32_16x16x32_f16 v[40:43], v[60:63], v[56:59], v[40:43]
	ds_read_b128 v[60:63], v105 offset:25536
	v_mov_b32_dpp v32, v107 row_newbcast:2 row_mask:0xf bank_mask:0x3
	v_mov_b32_dpp v32, v107 row_newbcast:10 row_mask:0xf bank_mask:0xc
	v_add_u32_e32 v33, v102, v33
	s_cmp_lg_u64 vcc, 0
	s_waitcnt lgkmcnt(2)
	v_mfma_f32_16x16x32_f16 v[44:47], v[52:55], v[56:59], v[44:47]
	v_mov_b32_dpp v52, v107 row_newbcast:3 row_mask:0xf bank_mask:0x3
	v_mov_b32_dpp v52, v107 row_newbcast:11 row_mask:0xf bank_mask:0xc
	v_mov_b32_dpp v53, v107 row_newbcast:4 row_mask:0xf bank_mask:0x3
	v_mov_b32_dpp v53, v107 row_newbcast:12 row_mask:0xf bank_mask:0xc
	v_add_u32_e32 v32, v102, v32
	ds_read_b128 v[76:79], v33 offset:52240
	ds_read_b128 v[72:75], v32 offset:52240
	s_waitcnt lgkmcnt(2)
	v_mfma_f32_16x16x32_f16 v[48:51], v[60:63], v[56:59], v[48:51]
	v_add_u32_e32 v32, v102, v52
	v_add_u32_e32 v33, v102, v53
	v_mov_b32_dpp v56, v107 row_newbcast:5 row_mask:0xf bank_mask:0x3
	v_mov_b32_dpp v56, v107 row_newbcast:13 row_mask:0xf bank_mask:0xc
	v_mov_b32_dpp v57, v107 row_newbcast:6 row_mask:0xf bank_mask:0x3
	v_mov_b32_dpp v57, v107 row_newbcast:14 row_mask:0xf bank_mask:0xc
	ds_read_b128 v[80:83], v32 offset:52240
	ds_read_b128 v[52:55], v33 offset:52240
	v_mov_b32_dpp v32, v107 row_newbcast:7 row_mask:0xf bank_mask:0x3
	v_mov_b32_dpp v32, v107 row_newbcast:15 row_mask:0xf bank_mask:0xc
	s_cselect_b64 s[22:23], -1, 0
	v_add_u32_e32 v33, v102, v56
	v_add_u32_e32 v56, v102, v57
	ds_read_b128 v[60:63], v33 offset:52240
	ds_read_b128 v[64:67], v56 offset:52240
	v_add_u32_e32 v32, v102, v32
	ds_read_b128 v[56:59], v32 offset:52240
	v_cmp_lt_i32_e64 s[6:7], 12, v35
	s_cbranch_vccz .LBB4_82
	v_mov_b32_dpp v0, v106 row_newbcast:0 row_mask:0xf bank_mask:0x3
	v_mov_b32_dpp v0, v106 row_newbcast:8 row_mask:0xf bank_mask:0xc
	v_mov_b32_dpp v1, v106 row_newbcast:1 row_mask:0xf bank_mask:0x3
	v_mov_b32_dpp v1, v106 row_newbcast:9 row_mask:0xf bank_mask:0xc
	v_mov_b32_dpp v16, v106 row_newbcast:2 row_mask:0xf bank_mask:0x3
	v_mov_b32_dpp v16, v106 row_newbcast:10 row_mask:0xf bank_mask:0xc
	v_mov_b32_dpp v17, v106 row_newbcast:3 row_mask:0xf bank_mask:0x3
	v_mov_b32_dpp v17, v106 row_newbcast:11 row_mask:0xf bank_mask:0xc
	v_add_u32_e32 v0, v102, v0
	v_add_u32_e32 v8, v102, v1
	v_add_u32_e32 v16, v102, v16
	v_add_u32_e32 v24, v102, v17
	ds_read_b128 v[0:3], v0 offset:52240
	ds_read_b128 v[8:11], v8 offset:52240
	ds_read_b128 v[16:19], v16 offset:52240
	ds_read_b128 v[24:27], v24 offset:52240
.LBB4_82:
	s_cmp_lg_u64 s[6:7], 0
	s_cselect_b64 s[26:27], -1, 0
	s_cmp_eq_u64 s[6:7], 0
	s_cbranch_scc1 .LBB4_84
	v_mov_b32_dpp v4, v106 row_newbcast:4 row_mask:0xf bank_mask:0x3
	v_mov_b32_dpp v4, v106 row_newbcast:12 row_mask:0xf bank_mask:0xc
	v_mov_b32_dpp v5, v106 row_newbcast:5 row_mask:0xf bank_mask:0x3
	v_mov_b32_dpp v5, v106 row_newbcast:13 row_mask:0xf bank_mask:0xc
	v_mov_b32_dpp v20, v106 row_newbcast:6 row_mask:0xf bank_mask:0x3
	v_mov_b32_dpp v20, v106 row_newbcast:14 row_mask:0xf bank_mask:0xc
	v_mov_b32_dpp v21, v106 row_newbcast:7 row_mask:0xf bank_mask:0x3
	v_mov_b32_dpp v21, v106 row_newbcast:15 row_mask:0xf bank_mask:0xc
	v_add_u32_e32 v4, v102, v4
	v_add_u32_e32 v12, v102, v5
	v_add_u32_e32 v20, v102, v20
	v_add_u32_e32 v28, v102, v21
	ds_read_b128 v[4:7], v4 offset:52240
	ds_read_b128 v[12:15], v12 offset:52240
	ds_read_b128 v[20:23], v20 offset:52240
	ds_read_b128 v[28:31], v28 offset:52240
.LBB4_84:
	v_cvt_f32_i32_e32 v32, v35
	v_max_f32_e32 v32, 1.0, v32
	v_div_scale_f32 v33, s[6:7], v32, v32, 1.0
	v_rcp_f32_e32 v84, v33
	v_div_scale_f32 v85, vcc, 1.0, v32, 1.0
	v_fma_f32 v86, -v33, v84, 1.0
	v_fmac_f32_e32 v84, v86, v84
	v_mul_f32_e32 v86, v85, v84
	v_fma_f32 v87, -v33, v86, v85
	v_fmac_f32_e32 v86, v87, v84
	v_fma_f32 v33, -v33, v86, v85
	v_div_fmas_f32 v33, v33, v84, v86
	v_div_fixup_f32 v32, v33, v32, 1.0
	v_cvt_f16_f32_e32 v33, v32
	v_cvt_pk_f16_f32 v32, v32, v32
	s_andn2_b64 vcc, exec, s[22:23]
	v_pk_fma_f16 v68, v33, v68, 0 op_sel_hi:[0,1,1]
	v_pk_fma_f16 v69, v33, v69, 0 op_sel_hi:[0,1,1]
	v_pk_fma_f16 v70, v33, v70, 0 op_sel_hi:[0,1,1]
	v_pk_fma_f16 v71, v33, v71, 0 op_sel_hi:[0,1,1]
	s_waitcnt lgkmcnt(6)
	v_pk_fma_f16 v71, v33, v79, v71 op_sel_hi:[0,1,1]
	v_pk_fma_f16 v70, v33, v78, v70 op_sel_hi:[0,1,1]
	v_pk_fma_f16 v69, v33, v77, v69 op_sel_hi:[0,1,1]
	v_pk_fma_f16 v68, v33, v76, v68 op_sel_hi:[0,1,1]
	s_waitcnt lgkmcnt(5)
	v_pk_fma_f16 v68, v33, v72, v68 op_sel_hi:[0,1,1]
	v_pk_fma_f16 v69, v33, v73, v69 op_sel_hi:[0,1,1]
	v_pk_fma_f16 v70, v33, v74, v70 op_sel_hi:[0,1,1]
	v_pk_fma_f16 v71, v33, v75, v71 op_sel_hi:[0,1,1]
	s_waitcnt lgkmcnt(4)
	v_pk_fma_f16 v71, v33, v83, v71 op_sel_hi:[0,1,1]
	v_pk_fma_f16 v70, v33, v82, v70 op_sel_hi:[0,1,1]
	v_pk_fma_f16 v69, v33, v81, v69 op_sel_hi:[0,1,1]
	v_pk_fma_f16 v68, v33, v80, v68 op_sel_hi:[0,1,1]
	s_waitcnt lgkmcnt(3)
	v_pk_fma_f16 v68, v33, v52, v68 op_sel_hi:[0,1,1]
	v_pk_fma_f16 v69, v33, v53, v69 op_sel_hi:[0,1,1]
	v_pk_fma_f16 v70, v33, v54, v70 op_sel_hi:[0,1,1]
	v_pk_fma_f16 v71, v33, v55, v71 op_sel_hi:[0,1,1]
	s_waitcnt lgkmcnt(2)
	v_pk_fma_f16 v71, v33, v63, v71 op_sel_hi:[0,1,1]
	v_pk_fma_f16 v70, v33, v62, v70 op_sel_hi:[0,1,1]
	v_pk_fma_f16 v69, v33, v61, v69 op_sel_hi:[0,1,1]
	v_pk_fma_f16 v68, v33, v60, v68 op_sel_hi:[0,1,1]
	s_waitcnt lgkmcnt(1)
	v_pk_fma_f16 v68, v33, v64, v68 op_sel_hi:[0,1,1]
	v_pk_fma_f16 v69, v33, v65, v69 op_sel_hi:[0,1,1]
	v_pk_fma_f16 v70, v33, v66, v70 op_sel_hi:[0,1,1]
	v_pk_fma_f16 v71, v33, v67, v71 op_sel_hi:[0,1,1]
	s_waitcnt lgkmcnt(0)
	v_pk_fma_f16 v71, v33, v59, v71 op_sel_hi:[0,1,1]
	v_pk_fma_f16 v70, v33, v58, v70 op_sel_hi:[0,1,1]
	v_pk_fma_f16 v69, v33, v57, v69 op_sel_hi:[0,1,1]
	v_pk_fma_f16 v68, v33, v56, v68 op_sel_hi:[0,1,1]
	s_cbranch_vccnz .LBB4_86
	v_pk_fma_f16 v33, v32, v0, v68
	v_pk_fma_f16 v68, v32, v1, v69
	v_pk_fma_f16 v69, v32, v2, v70
	v_pk_fma_f16 v70, v32, v3, v71
	v_pk_fma_f16 v69, v32, v10, v69
	v_pk_fma_f16 v70, v32, v11, v70
	v_pk_fma_f16 v68, v32, v9, v68
	v_pk_fma_f16 v33, v32, v8, v33
	v_pk_fma_f16 v68, v32, v17, v68
	v_pk_fma_f16 v33, v32, v16, v33
	v_pk_fma_f16 v69, v32, v18, v69
	v_pk_fma_f16 v70, v32, v19, v70
	s_nop 0
	v_pk_fma_f16 v71, v32, v27, v70
	v_pk_fma_f16 v70, v32, v26, v69
	v_pk_fma_f16 v69, v32, v25, v68
	v_pk_fma_f16 v68, v32, v24, v33

.LBB4_88:
	v_cmp_lt_i32_e32 vcc, 16, v35
	s_cbranch_vccz .LBB4_99
	v_mov_b32_dpp v33, v95 row_newbcast:0 row_mask:0xf bank_mask:0x3
	v_mov_b32_dpp v33, v95 row_newbcast:8 row_mask:0xf bank_mask:0xc
	v_mov_b32_dpp v72, v95 row_newbcast:1 row_mask:0xf bank_mask:0x3
	v_mov_b32_dpp v72, v95 row_newbcast:9 row_mask:0xf bank_mask:0xc
	v_mov_b32_dpp v73, v95 row_newbcast:2 row_mask:0xf bank_mask:0x3
	v_mov_b32_dpp v73, v95 row_newbcast:10 row_mask:0xf bank_mask:0xc
	v_mov_b32_dpp v74, v95 row_newbcast:3 row_mask:0xf bank_mask:0x3
	v_mov_b32_dpp v74, v95 row_newbcast:11 row_mask:0xf bank_mask:0xc
	v_cmp_lt_i32_e32 vcc, 20, v35
	v_add_u32_e32 v33, v102, v33
	v_add_u32_e32 v72, v102, v72
	ds_read_b128 v[84:87], v33 offset:52240
	ds_read_b128 v[80:83], v72 offset:52240
	v_add_u32_e32 v33, v102, v73
	v_add_u32_e32 v72, v102, v74
	ds_read_b128 v[76:79], v33 offset:52240
	ds_read_b128 v[72:75], v72 offset:52240
	s_cmp_lg_u64 vcc, 0
	s_cselect_b64 s[6:7], -1, 0
	s_cbranch_vccz .LBB4_91
	v_mov_b32_dpp v33, v95 row_newbcast:4 row_mask:0xf bank_mask:0x3
	v_mov_b32_dpp v33, v95 row_newbcast:12 row_mask:0xf bank_mask:0xc
	v_mov_b32_dpp v52, v95 row_newbcast:5 row_mask:0xf bank_mask:0x3
	v_mov_b32_dpp v52, v95 row_newbcast:13 row_mask:0xf bank_mask:0xc
	v_mov_b32_dpp v56, v95 row_newbcast:6 row_mask:0xf bank_mask:0x3
	v_mov_b32_dpp v56, v95 row_newbcast:14 row_mask:0xf bank_mask:0xc
	v_mov_b32_dpp v57, v95 row_newbcast:7 row_mask:0xf bank_mask:0x3
	v_mov_b32_dpp v57, v95 row_newbcast:15 row_mask:0xf bank_mask:0xc
	v_add_u32_e32 v33, v102, v33
	v_add_u32_e32 v58, v102, v52
	ds_read_b128 v[52:55], v33 offset:52240
	ds_read_b128 v[60:63], v58 offset:52240
	v_add_u32_e32 v33, v102, v56
	v_add_u32_e32 v56, v102, v57
	ds_read_b128 v[64:67], v33 offset:52240
	ds_read_b128 v[56:59], v56 offset:52240

.LBB4_94:
	s_waitcnt lgkmcnt(0)
	s_or_b64 exec, exec, s[6:7]
	s_nop 1
	v_mov_b32_dpp v52, v34 row_newbcast:0 row_mask:0xf bank_mask:0x3
	v_mov_b32_dpp v52, v34 row_newbcast:8 row_mask:0xf bank_mask:0xc
	v_mov_b32_dpp v53, v34 row_newbcast:1 row_mask:0xf bank_mask:0x3
	v_mov_b32_dpp v53, v34 row_newbcast:9 row_mask:0xf bank_mask:0xc
	v_mov_b32_dpp v60, v34 row_newbcast:2 row_mask:0xf bank_mask:0x3
	v_mov_b32_dpp v60, v34 row_newbcast:10 row_mask:0xf bank_mask:0xc
	v_mov_b32_dpp v61, v34 row_newbcast:3 row_mask:0xf bank_mask:0x3
	v_mov_b32_dpp v61, v34 row_newbcast:11 row_mask:0xf bank_mask:0xc
	v_mov_b32_dpp v72, v34 row_newbcast:4 row_mask:0xf bank_mask:0x3
	v_mov_b32_dpp v72, v34 row_newbcast:12 row_mask:0xf bank_mask:0xc
	v_mov_b32_dpp v73, v34 row_newbcast:5 row_mask:0xf bank_mask:0x3
	v_mov_b32_dpp v73, v34 row_newbcast:13 row_mask:0xf bank_mask:0xc
	v_mov_b32_dpp v80, v34 row_newbcast:6 row_mask:0xf bank_mask:0x3
	v_mov_b32_dpp v80, v34 row_newbcast:14 row_mask:0xf bank_mask:0xc
	v_mov_b32_dpp v34, v34 row_newbcast:7 row_mask:0xf bank_mask:0x3
	v_mov_b32_dpp v34, v34 row_newbcast:15 row_mask:0xf bank_mask:0xc
	v_add_u32_e32 v52, v102, v52
	v_add_u32_e32 v56, v102, v53
	ds_read_b128 v[52:55], v52 offset:52240
	ds_read_b128 v[56:59], v56 offset:52240
	v_add_u32_e32 v60, v102, v60
	v_add_u32_e32 v64, v102, v61
	ds_read_b128 v[60:63], v60 offset:52240
	ds_read_b128 v[64:67], v64 offset:52240
	v_add_u32_e32 v72, v102, v72
	v_add_u32_e32 v76, v102, v73
	v_add_u32_e32 v80, v102, v80
	v_add_u32_e32 v34, v102, v34
	ds_read_b128 v[72:75], v72 offset:52240
	ds_read_b128 v[76:79], v76 offset:52240
	ds_read_b128 v[80:83], v80 offset:52240
	ds_read_b128 v[84:87], v34 offset:52240
	s_waitcnt lgkmcnt(7)
	v_pk_fma_f16 v34, v32, v52, v68
	v_pk_fma_f16 v52, v32, v53, v69
	v_pk_fma_f16 v53, v32, v54, v70
	v_pk_fma_f16 v54, v32, v55, v71
	s_waitcnt lgkmcnt(6)
	v_pk_fma_f16 v53, v32, v58, v53
	v_pk_fma_f16 v54, v32, v59, v54
	v_pk_fma_f16 v52, v32, v57, v52
	v_pk_fma_f16 v34, v32, v56, v34
	s_waitcnt lgkmcnt(5)
	v_pk_fma_f16 v52, v32, v61, v52
	v_pk_fma_f16 v34, v32, v60, v34
	v_pk_fma_f16 v53, v32, v62, v53
	v_pk_fma_f16 v54, v32, v63, v54
	s_waitcnt lgkmcnt(4)
	v_pk_fma_f16 v53, v32, v66, v53
	v_pk_fma_f16 v54, v32, v67, v54
	v_pk_fma_f16 v52, v32, v65, v52
	v_pk_fma_f16 v34, v32, v64, v34
	s_waitcnt lgkmcnt(3)
	v_pk_fma_f16 v52, v32, v73, v52
	v_pk_fma_f16 v34, v32, v72, v34
	v_pk_fma_f16 v53, v32, v74, v53
	v_pk_fma_f16 v54, v32, v75, v54
	s_waitcnt lgkmcnt(2)
	v_pk_fma_f16 v53, v32, v78, v53
	v_pk_fma_f16 v54, v32, v79, v54
	v_pk_fma_f16 v52, v32, v77, v52
	v_pk_fma_f16 v34, v32, v76, v34
	s_waitcnt lgkmcnt(1)
	v_pk_fma_f16 v52, v32, v81, v52
	v_pk_fma_f16 v34, v32, v80, v34
	v_pk_fma_f16 v53, v32, v82, v53
	v_pk_fma_f16 v54, v32, v83, v54
	s_waitcnt lgkmcnt(0)
	v_pk_fma_f16 v70, v32, v86, v53
	v_pk_fma_f16 v71, v32, v87, v54
	v_pk_fma_f16 v69, v32, v85, v52
	v_pk_fma_f16 v68, v32, v84, v34
	s_add_i32 s22, s22, 8
.LBB4_95:
	s_waitcnt lgkmcnt(0)
	v_cmp_lt_i32_e32 vcc, s22, v35
	s_cbranch_vccz .LBB4_98
	v_add_u32_e32 v34, s22, v97
	v_cmp_lt_i32_e32 vcc, v34, v35
	v_mov_b32_e32 v34, 0x10000
	s_and_saveexec_b64 s[6:7], vcc
	s_cbranch_execz .LBB4_94
	v_add_u32_e32 v52, s22, v33
	v_ashrrev_i32_e32 v53, 31, v52
	v_lshl_add_u64 v[52:53], v[52:53], 2, s[12:13]
	global_load_dword v34, v[52:53], off
	s_waitcnt vmcnt(0)
	v_lshrrev_b32_e32 v34, 10, v34
	v_and_b32_e32 v34, 0x3fff80, v34
	s_branch .LBB4_94
